# v7 + P0 silu(c) staging: 18 loads in flight instead of 18 serialized round trips
# speedup vs baseline: 1.0052x; 1.0015x over previous
; __device__ __forceinline__ void p0_prologue(Frame& F, const InPtrs& A) {
;     ...
;         for (int it = blockIdx.x; it < 96; it += F.G) {
;             if (!have) {
;                 for (int i = F.tid; i < 9 * 1024; i += NTHREADS) { const int r = i >> 10, k = i & 1023; const float v = r < 8 ? A[I_C][r * 1024 + k] : A[I_CCTX][k]; sv[i] = v / (1.0f + __expf(-v)); }
;                 __syncthreads(); have = true;
.LBB0_12:
	s_and_b64 vcc, exec, s[6:7]
	s_cbranch_vccnz .LBB0_21
	s_and_saveexec_b64 s[6:7], s[4:5]
	s_cbranch_execz .LBB0_20
	v_mov_b32_e32 v2, s23
	v_mov_b32_e32 v3, s30
	ds_read_b32 v2, v2
	ds_read_b32 v3, v3
	v_mov_b32_e32 v4, s21
	v_mov_b32_e32 v5, s22
	ds_read_b32 v4, v4
	ds_read_b32 v5, v5
	s_waitcnt lgkmcnt(0)
	v_readfirstlane_b32 s42, v2
	v_readfirstlane_b32 s43, v3
	v_readfirstlane_b32 s46, v4
	v_readfirstlane_b32 s47, v5
	v_add_u32_e32 v85, 0x1000, v38
	v_add_u32_e32 v86, 0x2000, v38
	v_add_u32_e32 v87, 0x3000, v38
	v_add_u32_e32 v88, 0x4000, v38
	v_add_u32_e32 v89, 0x5000, v38
	v_add_u32_e32 v90, 0x6000, v38
	v_add_u32_e32 v91, 0x7000, v38
	s_nop 0
	global_load_dword v66, v38, s[42:43]
	global_load_dword v67, v38, s[42:43] offset:2048
	global_load_dword v68, v85, s[42:43]
	global_load_dword v69, v85, s[42:43] offset:2048
	global_load_dword v70, v86, s[42:43]
	global_load_dword v71, v86, s[42:43] offset:2048
	global_load_dword v72, v87, s[42:43]
	global_load_dword v73, v87, s[42:43] offset:2048
	global_load_dword v74, v88, s[42:43]
	global_load_dword v75, v88, s[42:43] offset:2048
	global_load_dword v76, v89, s[42:43]
	global_load_dword v77, v89, s[42:43] offset:2048
	global_load_dword v78, v90, s[42:43]
	global_load_dword v79, v90, s[42:43] offset:2048
	global_load_dword v80, v91, s[42:43]
	global_load_dword v81, v91, s[42:43] offset:2048
	global_load_dword v82, v38, s[46:47]
	global_load_dword v83, v38, s[46:47] offset:2048
	s_waitcnt vmcnt(17)
	v_mov_b32_e32 v2, v66
	v_mul_f32_e32 v3, 0xbfb8aa3b, v2
	v_exp_f32_e32 v3, v3
	s_nop 0
	v_add_f32_e32 v3, 1.0, v3
	v_div_scale_f32 v5, s[10:11], v3, v3, v2
	v_rcp_f32_e32 v7, v5
	v_div_scale_f32 v8, vcc, v2, v3, v2
	v_fma_f32 v9, -v5, v7, 1.0
	v_fmac_f32_e32 v7, v9, v7
	v_mul_f32_e32 v9, v8, v7
	v_fma_f32 v10, -v5, v9, v8
	v_fmac_f32_e32 v9, v10, v7
	v_fma_f32 v5, -v5, v9, v8
	v_div_fmas_f32 v5, v5, v7, v9
	v_div_fixup_f32 v2, v5, v3, v2
	ds_write_b32 v37, v2
	s_waitcnt vmcnt(16)
	v_mov_b32_e32 v2, v67
	v_mul_f32_e32 v3, 0xbfb8aa3b, v2
	v_exp_f32_e32 v3, v3
	s_nop 0
	v_add_f32_e32 v3, 1.0, v3
	v_div_scale_f32 v5, s[10:11], v3, v3, v2
	v_rcp_f32_e32 v7, v5
	v_div_scale_f32 v8, vcc, v2, v3, v2
	v_fma_f32 v9, -v5, v7, 1.0
	v_fmac_f32_e32 v7, v9, v7
	v_mul_f32_e32 v9, v8, v7
	v_fma_f32 v10, -v5, v9, v8
	v_fmac_f32_e32 v9, v10, v7
	v_fma_f32 v5, -v5, v9, v8
	v_div_fmas_f32 v5, v5, v7, v9
	v_div_fixup_f32 v2, v5, v3, v2
	ds_write_b32 v37, v2 offset:2048
	s_waitcnt vmcnt(15)
	v_mov_b32_e32 v2, v68
	v_mul_f32_e32 v3, 0xbfb8aa3b, v2
	v_exp_f32_e32 v3, v3
	s_nop 0
	v_add_f32_e32 v3, 1.0, v3
	v_div_scale_f32 v5, s[10:11], v3, v3, v2
	v_rcp_f32_e32 v7, v5
	v_div_scale_f32 v8, vcc, v2, v3, v2
	v_fma_f32 v9, -v5, v7, 1.0
	v_fmac_f32_e32 v7, v9, v7
	v_mul_f32_e32 v9, v8, v7
	v_fma_f32 v10, -v5, v9, v8
	v_fmac_f32_e32 v9, v10, v7
	v_fma_f32 v5, -v5, v9, v8
	v_div_fmas_f32 v5, v5, v7, v9
	v_div_fixup_f32 v2, v5, v3, v2
	ds_write_b32 v37, v2 offset:4096
	s_waitcnt vmcnt(14)
	v_mov_b32_e32 v2, v69
	v_mul_f32_e32 v3, 0xbfb8aa3b, v2
	v_exp_f32_e32 v3, v3
	s_nop 0
	v_add_f32_e32 v3, 1.0, v3
	v_div_scale_f32 v5, s[10:11], v3, v3, v2
	v_rcp_f32_e32 v7, v5
	v_div_scale_f32 v8, vcc, v2, v3, v2
	v_fma_f32 v9, -v5, v7, 1.0
	v_fmac_f32_e32 v7, v9, v7
	v_mul_f32_e32 v9, v8, v7
	v_fma_f32 v10, -v5, v9, v8
	v_fmac_f32_e32 v9, v10, v7
	v_fma_f32 v5, -v5, v9, v8
	v_div_fmas_f32 v5, v5, v7, v9
	v_div_fixup_f32 v2, v5, v3, v2
	ds_write_b32 v37, v2 offset:6144
	s_waitcnt vmcnt(13)
	v_mov_b32_e32 v2, v70
	v_mul_f32_e32 v3, 0xbfb8aa3b, v2
	v_exp_f32_e32 v3, v3
	s_nop 0
	v_add_f32_e32 v3, 1.0, v3
	v_div_scale_f32 v5, s[10:11], v3, v3, v2
	v_rcp_f32_e32 v7, v5
	v_div_scale_f32 v8, vcc, v2, v3, v2
	v_fma_f32 v9, -v5, v7, 1.0
	v_fmac_f32_e32 v7, v9, v7
	v_mul_f32_e32 v9, v8, v7
	v_fma_f32 v10, -v5, v9, v8
	v_fmac_f32_e32 v9, v10, v7
	v_fma_f32 v5, -v5, v9, v8
	v_div_fmas_f32 v5, v5, v7, v9
	v_div_fixup_f32 v2, v5, v3, v2
	ds_write_b32 v37, v2 offset:8192
	s_waitcnt vmcnt(12)
	v_mov_b32_e32 v2, v71
	v_mul_f32_e32 v3, 0xbfb8aa3b, v2
	v_exp_f32_e32 v3, v3
	s_nop 0
	v_add_f32_e32 v3, 1.0, v3
	v_div_scale_f32 v5, s[10:11], v3, v3, v2
	v_rcp_f32_e32 v7, v5
	v_div_scale_f32 v8, vcc, v2, v3, v2
	v_fma_f32 v9, -v5, v7, 1.0
	v_fmac_f32_e32 v7, v9, v7
	v_mul_f32_e32 v9, v8, v7
	v_fma_f32 v10, -v5, v9, v8
	v_fmac_f32_e32 v9, v10, v7
	v_fma_f32 v5, -v5, v9, v8
	v_div_fmas_f32 v5, v5, v7, v9
	v_div_fixup_f32 v2, v5, v3, v2
	ds_write_b32 v37, v2 offset:10240
	s_waitcnt vmcnt(11)
	v_mov_b32_e32 v2, v72
	v_mul_f32_e32 v3, 0xbfb8aa3b, v2
	v_exp_f32_e32 v3, v3
	s_nop 0
	v_add_f32_e32 v3, 1.0, v3
	v_div_scale_f32 v5, s[10:11], v3, v3, v2
	v_rcp_f32_e32 v7, v5
	v_div_scale_f32 v8, vcc, v2, v3, v2
	v_fma_f32 v9, -v5, v7, 1.0
	v_fmac_f32_e32 v7, v9, v7
	v_mul_f32_e32 v9, v8, v7
	v_fma_f32 v10, -v5, v9, v8
	v_fmac_f32_e32 v9, v10, v7
	v_fma_f32 v5, -v5, v9, v8
	v_div_fmas_f32 v5, v5, v7, v9
	v_div_fixup_f32 v2, v5, v3, v2
	ds_write_b32 v37, v2 offset:12288
	s_waitcnt vmcnt(10)
	v_mov_b32_e32 v2, v73
	v_mul_f32_e32 v3, 0xbfb8aa3b, v2
	v_exp_f32_e32 v3, v3
	s_nop 0
	v_add_f32_e32 v3, 1.0, v3
	v_div_scale_f32 v5, s[10:11], v3, v3, v2
	v_rcp_f32_e32 v7, v5
	v_div_scale_f32 v8, vcc, v2, v3, v2
	v_fma_f32 v9, -v5, v7, 1.0
	v_fmac_f32_e32 v7, v9, v7
	v_mul_f32_e32 v9, v8, v7
	v_fma_f32 v10, -v5, v9, v8
	v_fmac_f32_e32 v9, v10, v7
	v_fma_f32 v5, -v5, v9, v8
	v_div_fmas_f32 v5, v5, v7, v9
	v_div_fixup_f32 v2, v5, v3, v2
	ds_write_b32 v37, v2 offset:14336
	s_waitcnt vmcnt(9)
; __device__ __forceinline__ void p0_prologue(Frame& F, const InPtrs& A) {
;     ...
;                 for (int i = F.tid; i < 9 * 1024; i += NTHREADS) { const int r = i >> 10, k = i & 1023; const float v = r < 8 ? A[I_C][r * 1024 + k] : A[I_CCTX][k]; sv[i] = v / (1.0f + __expf(-v)); }
	v_mov_b32_e32 v2, v74
	v_mul_f32_e32 v3, 0xbfb8aa3b, v2
	v_exp_f32_e32 v3, v3
	s_nop 0
	v_add_f32_e32 v3, 1.0, v3
	v_div_scale_f32 v5, s[10:11], v3, v3, v2
	v_rcp_f32_e32 v7, v5
	v_div_scale_f32 v8, vcc, v2, v3, v2
	v_fma_f32 v9, -v5, v7, 1.0
	v_fmac_f32_e32 v7, v9, v7
	v_mul_f32_e32 v9, v8, v7
	v_fma_f32 v10, -v5, v9, v8
	v_fmac_f32_e32 v9, v10, v7
	v_fma_f32 v5, -v5, v9, v8
	v_div_fmas_f32 v5, v5, v7, v9
	v_div_fixup_f32 v2, v5, v3, v2
	ds_write_b32 v37, v2 offset:16384
	s_waitcnt vmcnt(8)
	v_mov_b32_e32 v2, v75
	v_mul_f32_e32 v3, 0xbfb8aa3b, v2
	v_exp_f32_e32 v3, v3
	s_nop 0
	v_add_f32_e32 v3, 1.0, v3
	v_div_scale_f32 v5, s[10:11], v3, v3, v2
	v_rcp_f32_e32 v7, v5
	v_div_scale_f32 v8, vcc, v2, v3, v2
	v_fma_f32 v9, -v5, v7, 1.0
	v_fmac_f32_e32 v7, v9, v7
	v_mul_f32_e32 v9, v8, v7
	v_fma_f32 v10, -v5, v9, v8
	v_fmac_f32_e32 v9, v10, v7
	v_fma_f32 v5, -v5, v9, v8
	v_div_fmas_f32 v5, v5, v7, v9
	v_div_fixup_f32 v2, v5, v3, v2
	ds_write_b32 v37, v2 offset:18432
	s_waitcnt vmcnt(7)
	v_mov_b32_e32 v2, v76
	v_mul_f32_e32 v3, 0xbfb8aa3b, v2
	v_exp_f32_e32 v3, v3
	s_nop 0
	v_add_f32_e32 v3, 1.0, v3
	v_div_scale_f32 v5, s[10:11], v3, v3, v2
	v_rcp_f32_e32 v7, v5
	v_div_scale_f32 v8, vcc, v2, v3, v2
	v_fma_f32 v9, -v5, v7, 1.0
	v_fmac_f32_e32 v7, v9, v7
	v_mul_f32_e32 v9, v8, v7
	v_fma_f32 v10, -v5, v9, v8
	v_fmac_f32_e32 v9, v10, v7
	v_fma_f32 v5, -v5, v9, v8
	v_div_fmas_f32 v5, v5, v7, v9
	v_div_fixup_f32 v2, v5, v3, v2
	ds_write_b32 v37, v2 offset:20480
	s_waitcnt vmcnt(6)
	v_mov_b32_e32 v2, v77
	v_mul_f32_e32 v3, 0xbfb8aa3b, v2
	v_exp_f32_e32 v3, v3
	s_nop 0
	v_add_f32_e32 v3, 1.0, v3
	v_div_scale_f32 v5, s[10:11], v3, v3, v2
	v_rcp_f32_e32 v7, v5
	v_div_scale_f32 v8, vcc, v2, v3, v2
	v_fma_f32 v9, -v5, v7, 1.0
	v_fmac_f32_e32 v7, v9, v7
	v_mul_f32_e32 v9, v8, v7
	v_fma_f32 v10, -v5, v9, v8
	v_fmac_f32_e32 v9, v10, v7
	v_fma_f32 v5, -v5, v9, v8
	v_div_fmas_f32 v5, v5, v7, v9
	v_div_fixup_f32 v2, v5, v3, v2
	ds_write_b32 v37, v2 offset:22528
	s_waitcnt vmcnt(5)
	v_mov_b32_e32 v2, v78
	v_mul_f32_e32 v3, 0xbfb8aa3b, v2
	v_exp_f32_e32 v3, v3
	s_nop 0
	v_add_f32_e32 v3, 1.0, v3
	v_div_scale_f32 v5, s[10:11], v3, v3, v2
	v_rcp_f32_e32 v7, v5
	v_div_scale_f32 v8, vcc, v2, v3, v2
	v_fma_f32 v9, -v5, v7, 1.0
	v_fmac_f32_e32 v7, v9, v7
	v_mul_f32_e32 v9, v8, v7
	v_fma_f32 v10, -v5, v9, v8
	v_fmac_f32_e32 v9, v10, v7
	v_fma_f32 v5, -v5, v9, v8
	v_div_fmas_f32 v5, v5, v7, v9
	v_div_fixup_f32 v2, v5, v3, v2
	ds_write_b32 v37, v2 offset:24576
	s_waitcnt vmcnt(4)
	v_mov_b32_e32 v2, v79
	v_mul_f32_e32 v3, 0xbfb8aa3b, v2
	v_exp_f32_e32 v3, v3
	s_nop 0
	v_add_f32_e32 v3, 1.0, v3
	v_div_scale_f32 v5, s[10:11], v3, v3, v2
	v_rcp_f32_e32 v7, v5
	v_div_scale_f32 v8, vcc, v2, v3, v2
	v_fma_f32 v9, -v5, v7, 1.0
	v_fmac_f32_e32 v7, v9, v7
	v_mul_f32_e32 v9, v8, v7
	v_fma_f32 v10, -v5, v9, v8
	v_fmac_f32_e32 v9, v10, v7
	v_fma_f32 v5, -v5, v9, v8
	v_div_fmas_f32 v5, v5, v7, v9
	v_div_fixup_f32 v2, v5, v3, v2
	ds_write_b32 v37, v2 offset:26624
	s_waitcnt vmcnt(3)
	v_mov_b32_e32 v2, v80
	v_mul_f32_e32 v3, 0xbfb8aa3b, v2
	v_exp_f32_e32 v3, v3
	s_nop 0
	v_add_f32_e32 v3, 1.0, v3
	v_div_scale_f32 v5, s[10:11], v3, v3, v2
	v_rcp_f32_e32 v7, v5
	v_div_scale_f32 v8, vcc, v2, v3, v2
	v_fma_f32 v9, -v5, v7, 1.0
	v_fmac_f32_e32 v7, v9, v7
	v_mul_f32_e32 v9, v8, v7
	v_fma_f32 v10, -v5, v9, v8
	v_fmac_f32_e32 v9, v10, v7
	v_fma_f32 v5, -v5, v9, v8
	v_div_fmas_f32 v5, v5, v7, v9
	v_div_fixup_f32 v2, v5, v3, v2
	ds_write_b32 v37, v2 offset:28672
	s_waitcnt vmcnt(2)
	v_mov_b32_e32 v2, v81
	v_mul_f32_e32 v3, 0xbfb8aa3b, v2
	v_exp_f32_e32 v3, v3
	s_nop 0
	v_add_f32_e32 v3, 1.0, v3
	v_div_scale_f32 v5, s[10:11], v3, v3, v2
	v_rcp_f32_e32 v7, v5
	v_div_scale_f32 v8, vcc, v2, v3, v2
	v_fma_f32 v9, -v5, v7, 1.0
	v_fmac_f32_e32 v7, v9, v7
	v_mul_f32_e32 v9, v8, v7
	v_fma_f32 v10, -v5, v9, v8
	v_fmac_f32_e32 v9, v10, v7
	v_fma_f32 v5, -v5, v9, v8
	v_div_fmas_f32 v5, v5, v7, v9
	v_div_fixup_f32 v2, v5, v3, v2
	ds_write_b32 v37, v2 offset:30720
	s_waitcnt vmcnt(1)
	v_mov_b32_e32 v2, v82
	v_mul_f32_e32 v3, 0xbfb8aa3b, v2
	v_exp_f32_e32 v3, v3
	s_nop 0
	v_add_f32_e32 v3, 1.0, v3
	v_div_scale_f32 v5, s[10:11], v3, v3, v2
	v_rcp_f32_e32 v7, v5
	v_div_scale_f32 v8, vcc, v2, v3, v2
	v_fma_f32 v9, -v5, v7, 1.0
	v_fmac_f32_e32 v7, v9, v7
	v_mul_f32_e32 v9, v8, v7
	v_fma_f32 v10, -v5, v9, v8
	v_fmac_f32_e32 v9, v10, v7
	v_fma_f32 v5, -v5, v9, v8
	v_div_fmas_f32 v5, v5, v7, v9
	v_div_fixup_f32 v2, v5, v3, v2
	ds_write_b32 v37, v2 offset:32768
	s_waitcnt vmcnt(0)
	v_mov_b32_e32 v2, v83
	v_mul_f32_e32 v3, 0xbfb8aa3b, v2
	v_exp_f32_e32 v3, v3
	s_nop 0
	v_add_f32_e32 v3, 1.0, v3
	v_div_scale_f32 v5, s[10:11], v3, v3, v2
	v_rcp_f32_e32 v7, v5
	v_div_scale_f32 v8, vcc, v2, v3, v2
	v_fma_f32 v9, -v5, v7, 1.0
	v_fmac_f32_e32 v7, v9, v7
	v_mul_f32_e32 v9, v8, v7
	v_fma_f32 v10, -v5, v9, v8
	v_fmac_f32_e32 v9, v10, v7
	v_fma_f32 v5, -v5, v9, v8
	v_div_fmas_f32 v5, v5, v7, v9
	v_div_fixup_f32 v2, v5, v3, v2
	ds_write_b32 v37, v2 offset:34816
